# v21 plus scalar m-is-zero flag, hidden sum-check latency, shorter pads, leaner KV DMA issue blocks
# speedup vs baseline: 1.0302x; 1.0021x over previous
; template <int layer>
; __device__ __forceinline__ void attn_phase(LAS unsigned char* lds) {
;     ...
;             float m_reg = 0.f, l_reg = 0.f; f32x16 o[4];
; #pragma unroll
;             for (int d0 = 0; d0 < 4; ++d0)
; #pragma unroll
;                 for (int r = 0; r < 16; ++r) o[d0][r] = 0.f;
.LBB0_531:
	v_mov_b32_e32 v16, v3
	v_mov_b32_e32 v17, v3
	v_mov_b32_e32 v2, v3
	v_mov_b32_e32 v4, v3
	v_mov_b32_e32 v5, v3
	v_mov_b32_e32 v6, v3
	v_mov_b32_e32 v7, v3
	v_mov_b32_e32 v8, v3
	v_mov_b32_e32 v9, v3
	v_mov_b32_e32 v10, v3
	v_mov_b32_e32 v11, v3
	v_mov_b32_e32 v12, v3
	v_mov_b32_e32 v13, v3
	v_mov_b32_e32 v14, v3
	v_mov_b32_e32 v15, v3
	v_mov_b64_e32 v[66:67], v[16:17]
	v_mov_b64_e32 v[50:51], v[16:17]
	v_mov_b64_e32 v[34:35], v[16:17]
	s_lshr_b32 s29, s8, 6
	v_readlane_b32 s52, v252, 35
	v_readlane_b32 s54, v252, 33
	v_mov_b64_e32 v[64:65], v[14:15]
	v_mov_b64_e32 v[62:63], v[12:13]
	v_mov_b64_e32 v[60:61], v[10:11]
	v_mov_b64_e32 v[58:59], v[8:9]
	v_mov_b64_e32 v[56:57], v[6:7]
	v_mov_b64_e32 v[54:55], v[4:5]
	v_mov_b64_e32 v[52:53], v[2:3]
	v_mov_b64_e32 v[48:49], v[14:15]
	v_mov_b64_e32 v[46:47], v[12:13]
	v_mov_b64_e32 v[44:45], v[10:11]
	v_mov_b64_e32 v[42:43], v[8:9]
	v_mov_b64_e32 v[40:41], v[6:7]
	v_mov_b64_e32 v[38:39], v[4:5]
	v_mov_b64_e32 v[36:37], v[2:3]
	v_mov_b64_e32 v[32:33], v[14:15]
	v_mov_b64_e32 v[30:31], v[12:13]
	v_mov_b64_e32 v[28:29], v[10:11]
	v_mov_b64_e32 v[26:27], v[8:9]
	v_mov_b64_e32 v[24:25], v[6:7]
	v_mov_b64_e32 v[22:23], v[4:5]
	v_mov_b64_e32 v[20:21], v[2:3]
	v_mov_b64_e32 v[18:19], v[16:17]
	s_xor_b64 s[48:49], s[6:7], -1
	s_add_i32 s29, s29, 4
	s_or_b32 s16, s28, 31
	v_add_u32_e32 v220, s8, v215
	s_mov_b32 s17, 0
	v_mov_b32_e32 v223, 0
	s_mov_b32 s101, 1
	s_mov_b32 s63, 63
	s_mov_b64 s[50:51], s[46:47]
	v_readlane_b32 s53, v252, 36
	v_readlane_b32 s55, v252, 34
	v_mov_b64_e32 v[16:17], v[14:15]
	v_mov_b64_e32 v[14:15], v[12:13]
	v_mov_b64_e32 v[12:13], v[10:11]
	v_mov_b64_e32 v[10:11], v[8:9]
	v_mov_b64_e32 v[8:9], v[6:7]
	v_mov_b64_e32 v[6:7], v[4:5]
	v_mov_b64_e32 v[4:5], v[2:3]
	v_mov_b32_e32 v221, 0
	s_mov_b32 s58, 0
	s_branch .LBB0_534

.LBB0_536:
	s_or_b32 s6, s58, 1
	s_cmp_ge_u32 s6, s29
	s_waitcnt lgkmcnt(0)
	s_barrier
	s_cselect_b64 s[6:7], -1, 0
	s_xor_b64 s[56:57], s[18:19], -1
	s_or_b64 s[6:7], s[56:57], s[6:7]
	s_and_b64 vcc, exec, s[6:7]
	s_cbranch_vccnz .LBB0_538
	s_add_u32 s6, s50, 0xfff80000
	s_addc_u32 s7, s51, -1
	s_mov_b32 m0, s68
	s_nop 0
	global_load_lds_dwordx4 v1, s[6:7]
	s_mov_b32 m0, s79
	s_nop 0
	global_load_lds_dwordx4 v208, s[6:7]
	s_mov_b32 m0, s80
	s_nop 0
	global_load_lds_dwordx4 v209, s[6:7]
	s_mov_b32 m0, s81
	s_nop 0
	global_load_lds_dwordx4 v210, s[6:7]
	s_add_u32 s6, s54, 0xffffe000
	s_addc_u32 s7, s55, -1
	s_mov_b32 m0, s69
	s_nop 0
	global_load_lds_dwordx4 v188, s[6:7]
	s_mov_b32 m0, s82
	s_nop 0
	global_load_lds_dwordx4 v211, s[6:7]
	s_add_u32 s6, s52, 0xfff80000
	s_addc_u32 s7, s53, -1
	s_mov_b32 m0, s70
	s_nop 0
	global_load_lds_dwordx4 v181, s[6:7]
	s_mov_b32 m0, s83
	s_nop 0
	global_load_lds_dwordx4 v212, s[6:7]
	s_mov_b32 m0, s84
	s_nop 0
	global_load_lds_dwordx4 v213, s[6:7]
	s_mov_b32 m0, s85
	s_nop 0
	global_load_lds_dwordx4 v214, s[6:7]

.LBB0_544:
	s_add_i32 s58, s58, 2
	s_cmp_ge_u32 s58, s29
	s_cselect_b64 s[8:9], -1, 0
	s_cmp_lt_u32 s58, s29
	s_waitcnt lgkmcnt(0)
	s_barrier
	s_cselect_b64 s[40:41], -1, 0
	s_and_b64 s[40:41], s[18:19], s[40:41]
	s_andn2_b64 vcc, exec, s[40:41]
	s_cbranch_vccnz .LBB0_546
	s_mov_b32 m0, s65
	s_nop 0
	global_load_lds_dwordx4 v1, s[50:51]
	s_mov_b32 m0, s73
	s_nop 0
	global_load_lds_dwordx4 v208, s[50:51]
	s_mov_b32 m0, s74
	s_nop 0
	global_load_lds_dwordx4 v209, s[50:51]
	s_mov_b32 m0, s75
	s_nop 0
	global_load_lds_dwordx4 v210, s[50:51]
	s_mov_b32 m0, s66
	s_nop 0
	global_load_lds_dwordx4 v188, s[54:55]
	s_mov_b32 m0, s76
	s_nop 0
	global_load_lds_dwordx4 v211, s[54:55]
	s_mov_b32 m0, s67
	s_nop 0
	global_load_lds_dwordx4 v181, s[52:53]
	s_mov_b32 m0, s64
	s_nop 0
	global_load_lds_dwordx4 v212, s[52:53]
	s_mov_b32 m0, s77
	s_nop 0
	global_load_lds_dwordx4 v213, s[52:53]
	s_mov_b32 m0, s78
	s_nop 0
	global_load_lds_dwordx4 v214, s[52:53]

.LBB0_556:
	s_cmp_le_i32 s63, s28
	s_cbranch_scc0 .Lorig_a0b0
	s_cmp_eq_u32 s17, 0
	s_cbranch_scc1 .Lorig_a0b0
	s_setprio 3
	ds_read_b128 v[116:119], v189 offset:0
	ds_read_b128 v[120:123], v226 offset:0
	ds_read_b128 v[124:127], v227 offset:0
	ds_read_b128 v[128:131], v228 offset:0
	s_waitcnt lgkmcnt(3)
	v_mfma_f32_32x32x16_bf16 v[84:99], v[116:119], v[132:135], 0
	ds_read_b128 v[116:119], v232 offset:0
	s_waitcnt lgkmcnt(3)
	v_mfma_f32_32x32x16_bf16 v[84:99], v[120:123], v[136:139], v[84:99]
	ds_read_b128 v[120:123], v233 offset:0
	s_waitcnt lgkmcnt(3)
	v_mfma_f32_32x32x16_bf16 v[84:99], v[124:127], v[140:143], v[84:99]
	ds_read_b128 v[124:127], v234 offset:0
	s_waitcnt lgkmcnt(3)
	v_mfma_f32_32x32x16_bf16 v[84:99], v[128:131], v[144:147], v[84:99]
	ds_read_b128 v[128:131], v235 offset:0
	s_waitcnt lgkmcnt(3)
	v_mfma_f32_32x32x16_bf16 v[84:99], v[116:119], v[148:151], v[84:99]
	ds_read_b128 v[116:119], v190 offset:0
	s_waitcnt lgkmcnt(3)
	v_mfma_f32_32x32x16_bf16 v[84:99], v[120:123], v[152:155], v[84:99]
	ds_read_b128 v[120:123], v229 offset:0
	s_waitcnt lgkmcnt(3)
	v_mfma_f32_32x32x16_bf16 v[84:99], v[124:127], v[156:159], v[84:99]
	ds_read_b128 v[124:127], v230 offset:0
	s_waitcnt lgkmcnt(3)
	v_mfma_f32_32x32x16_bf16 v[84:99], v[128:131], v[160:163], v[84:99]
	ds_read_b128 v[128:131], v231 offset:0
	s_waitcnt lgkmcnt(3)
	v_mfma_f32_32x32x16_bf16 v[84:99], v[116:119], v[164:167], v[84:99]
	ds_read_b128 v[116:119], v189 offset:8192
	s_waitcnt lgkmcnt(3)
	v_mfma_f32_32x32x16_bf16 v[84:99], v[120:123], v[172:175], v[84:99]
	ds_read_b128 v[120:123], v226 offset:8192
	s_waitcnt lgkmcnt(3)
	v_mfma_f32_32x32x16_bf16 v[84:99], v[124:127], v[168:171], v[84:99]
	ds_read_b128 v[124:127], v227 offset:8192
	s_waitcnt lgkmcnt(3)
	v_mfma_f32_32x32x16_bf16 v[84:99], v[128:131], v[176:179], v[84:99]
	ds_read_b128 v[128:131], v228 offset:8192
	s_waitcnt lgkmcnt(3)
	v_mfma_f32_32x32x16_bf16 v[68:83], v[116:119], v[132:135], 0
	ds_read_b128 v[116:119], v232 offset:8192
	s_waitcnt lgkmcnt(3)
	v_mfma_f32_32x32x16_bf16 v[68:83], v[120:123], v[136:139], v[68:83]
	ds_read_b128 v[120:123], v233 offset:8192
	s_waitcnt lgkmcnt(3)
	v_mfma_f32_32x32x16_bf16 v[68:83], v[124:127], v[140:143], v[68:83]
	ds_read_b128 v[124:127], v234 offset:8192
	s_waitcnt lgkmcnt(3)
	v_mfma_f32_32x32x16_bf16 v[68:83], v[128:131], v[144:147], v[68:83]
	ds_read_b128 v[128:131], v235 offset:8192
	s_waitcnt lgkmcnt(3)
	v_mfma_f32_32x32x16_bf16 v[68:83], v[116:119], v[148:151], v[68:83]
	ds_read_b128 v[116:119], v190 offset:4096
	s_waitcnt lgkmcnt(3)
	v_mfma_f32_32x32x16_bf16 v[68:83], v[120:123], v[152:155], v[68:83]
	ds_read_b128 v[120:123], v229 offset:4096
	s_waitcnt lgkmcnt(3)
	v_mfma_f32_32x32x16_bf16 v[68:83], v[124:127], v[156:159], v[68:83]
	ds_read_b128 v[124:127], v230 offset:4096
	s_waitcnt lgkmcnt(3)
	v_mfma_f32_32x32x16_bf16 v[68:83], v[128:131], v[160:163], v[68:83]
	ds_read_b128 v[128:131], v231 offset:4096
	s_waitcnt lgkmcnt(3)
	v_mfma_f32_32x32x16_bf16 v[68:83], v[116:119], v[164:167], v[68:83]
	s_waitcnt lgkmcnt(2)
	v_mfma_f32_32x32x16_bf16 v[68:83], v[120:123], v[172:175], v[68:83]
	s_waitcnt lgkmcnt(1)
	v_mfma_f32_32x32x16_bf16 v[68:83], v[124:127], v[168:171], v[68:83]
	s_waitcnt lgkmcnt(0)
	v_mfma_f32_32x32x16_bf16 v[68:83], v[128:131], v[176:179], v[68:83]
	ds_read_b64_tr_b16 v[116:117], v191 offset:0
	ds_read_b64_tr_b16 v[118:119], v191 offset:2048
	ds_read_b64_tr_b16 v[120:121], v191 offset:4096
	ds_read_b64_tr_b16 v[122:123], v191 offset:6144
	ds_read_b64_tr_b16 v[124:125], v191 offset:8192
	ds_read_b64_tr_b16 v[126:127], v191 offset:10240
	ds_read_b64_tr_b16 v[128:129], v191 offset:12288
	ds_read_b64_tr_b16 v[130:131], v191 offset:14336
	s_setprio 0
	s_nop 2
	s_cmp_eq_u32 s101, 1
	s_cbranch_scc0 .Lsub_a0b0
	v_exp_f32_e32 v100, v84
	v_exp_f32_e32 v101, v85
	v_exp_f32_e32 v102, v86
	v_exp_f32_e32 v103, v87
	v_exp_f32_e32 v104, v88
	v_exp_f32_e32 v105, v89
	v_exp_f32_e32 v106, v90
	v_exp_f32_e32 v107, v91
	v_exp_f32_e32 v108, v92
	v_exp_f32_e32 v109, v93
	v_exp_f32_e32 v110, v94
	v_exp_f32_e32 v111, v95
	v_exp_f32_e32 v112, v96
	v_exp_f32_e32 v113, v97
	v_exp_f32_e32 v114, v98
	v_exp_f32_e32 v115, v99
	v_add_f32_e32 v237, v100, v101
	v_add_f32_e32 v251, v102, v103
	v_add_f32_e32 v237, v237, v104
	v_add_f32_e32 v251, v251, v105
	v_add_f32_e32 v237, v237, v106
	v_add_f32_e32 v251, v251, v107
	v_add_f32_e32 v237, v237, v108
	v_add_f32_e32 v251, v251, v109
	v_add_f32_e32 v237, v237, v110
	v_add_f32_e32 v251, v251, v111
	v_add_f32_e32 v237, v237, v112
	v_add_f32_e32 v251, v251, v113
	v_add_f32_e32 v237, v237, v114
	v_add_f32_e32 v251, v251, v115
	v_add_f32_e32 v237, v237, v251
	v_cvt_pk_bf16_f32 v238, v100, v101
	v_cvt_pk_bf16_f32 v239, v102, v103
	v_cvt_pk_bf16_f32 v240, v104, v105
	v_cvt_pk_bf16_f32 v241, v106, v107
	v_cvt_pk_bf16_f32 v242, v108, v109
	v_cvt_pk_bf16_f32 v243, v110, v111
	v_cvt_pk_bf16_f32 v244, v112, v113
	v_cvt_pk_bf16_f32 v245, v114, v115
	s_nop 1
	v_permlane32_swap_b32_e32 v238, v240
	v_permlane32_swap_b32_e32 v239, v241
	v_permlane32_swap_b32_e32 v242, v244
	v_permlane32_swap_b32_e32 v243, v245
	v_exp_f32_e32 v100, v68
	v_exp_f32_e32 v101, v69
	v_exp_f32_e32 v102, v70
	v_exp_f32_e32 v103, v71
	v_exp_f32_e32 v104, v72
	v_exp_f32_e32 v105, v73
	v_exp_f32_e32 v106, v74
	v_exp_f32_e32 v107, v75
	v_exp_f32_e32 v108, v76
	v_exp_f32_e32 v109, v77
	v_exp_f32_e32 v110, v78
	v_exp_f32_e32 v111, v79
	v_exp_f32_e32 v112, v80
	v_exp_f32_e32 v113, v81
	v_exp_f32_e32 v114, v82
	v_exp_f32_e32 v115, v83
	v_add_f32_e32 v250, v100, v101
	v_add_f32_e32 v251, v102, v103
	v_add_f32_e32 v250, v250, v104
	v_add_f32_e32 v251, v251, v105
	v_add_f32_e32 v250, v250, v106
	v_add_f32_e32 v251, v251, v107
	v_add_f32_e32 v250, v250, v108
	v_add_f32_e32 v251, v251, v109
	v_add_f32_e32 v250, v250, v110
	v_add_f32_e32 v251, v251, v111
	v_add_f32_e32 v250, v250, v112
	v_add_f32_e32 v251, v251, v113
	v_add_f32_e32 v250, v250, v114
	v_add_f32_e32 v251, v251, v115
	v_add_f32_e32 v250, v250, v251
	v_cvt_pk_bf16_f32 v100, v100, v101
	v_cvt_pk_bf16_f32 v101, v102, v103
	v_cvt_pk_bf16_f32 v102, v104, v105
	v_cvt_pk_bf16_f32 v103, v106, v107
	v_cvt_pk_bf16_f32 v104, v108, v109
	v_cvt_pk_bf16_f32 v105, v110, v111
	v_cvt_pk_bf16_f32 v106, v112, v113
	v_cvt_pk_bf16_f32 v107, v114, v115
	s_nop 1
	v_permlane32_swap_b32_e32 v100, v102
	v_permlane32_swap_b32_e32 v101, v103
	v_permlane32_swap_b32_e32 v104, v106
	v_permlane32_swap_b32_e32 v105, v107
	s_branch .Lsum_a0b0

.Lsum_a0b0:
	v_add_f32_e32 v237, v237, v250
	v_cmp_gt_f32_e32 vcc, 0x5f800000, v237
	v_mov_b32_e32 v250, v237
	s_nop 1
	v_permlane32_swap_b32_e32 v237, v250
	v_add_f32_e32 v237, v237, v250
	s_cmp_eq_u64 vcc, exec
	s_cbranch_scc0 .Lfb_a0b0
	v_add_f32_e32 v221, v237, v221
	v_mov_b32_e32 v222, v223
	s_setprio 3
	s_waitcnt lgkmcnt(6)
	v_mfma_f32_32x32x16_bf16 v[52:67], v[116:119], v[238:241], v[52:67]
	ds_read_b64_tr_b16 v[116:117], v191 offset:512
	ds_read_b64_tr_b16 v[118:119], v191 offset:2560
	s_waitcnt lgkmcnt(6)
	v_mfma_f32_32x32x16_bf16 v[52:67], v[120:123], v[242:245], v[52:67]
	ds_read_b64_tr_b16 v[120:121], v191 offset:4608
	ds_read_b64_tr_b16 v[122:123], v191 offset:6656
	s_waitcnt lgkmcnt(6)
	v_mfma_f32_32x32x16_bf16 v[52:67], v[124:127], v[100:103], v[52:67]
	ds_read_b64_tr_b16 v[124:125], v191 offset:8704
	ds_read_b64_tr_b16 v[126:127], v191 offset:10752
	s_waitcnt lgkmcnt(6)
	v_mfma_f32_32x32x16_bf16 v[52:67], v[128:131], v[104:107], v[52:67]
	ds_read_b64_tr_b16 v[128:129], v191 offset:12800
	ds_read_b64_tr_b16 v[130:131], v191 offset:14848
	s_waitcnt lgkmcnt(6)
	v_mfma_f32_32x32x16_bf16 v[36:51], v[116:119], v[238:241], v[36:51]
	ds_read_b64_tr_b16 v[116:117], v191 offset:1024
	ds_read_b64_tr_b16 v[118:119], v191 offset:3072
	s_waitcnt lgkmcnt(6)
	v_mfma_f32_32x32x16_bf16 v[36:51], v[120:123], v[242:245], v[36:51]
	ds_read_b64_tr_b16 v[120:121], v191 offset:5120
	ds_read_b64_tr_b16 v[122:123], v191 offset:7168
	s_waitcnt lgkmcnt(6)
	v_mfma_f32_32x32x16_bf16 v[36:51], v[124:127], v[100:103], v[36:51]
	ds_read_b64_tr_b16 v[124:125], v191 offset:9216
	ds_read_b64_tr_b16 v[126:127], v191 offset:11264
	s_waitcnt lgkmcnt(6)
	v_mfma_f32_32x32x16_bf16 v[36:51], v[128:131], v[104:107], v[36:51]
	ds_read_b64_tr_b16 v[128:129], v191 offset:13312
	ds_read_b64_tr_b16 v[130:131], v191 offset:15360
	s_waitcnt lgkmcnt(6)
	v_mfma_f32_32x32x16_bf16 v[20:35], v[116:119], v[238:241], v[20:35]
	ds_read_b64_tr_b16 v[116:117], v191 offset:1536
	ds_read_b64_tr_b16 v[118:119], v191 offset:3584
	s_waitcnt lgkmcnt(6)
	v_mfma_f32_32x32x16_bf16 v[20:35], v[120:123], v[242:245], v[20:35]
	ds_read_b64_tr_b16 v[120:121], v191 offset:5632
	ds_read_b64_tr_b16 v[122:123], v191 offset:7680
	s_waitcnt lgkmcnt(6)
	v_mfma_f32_32x32x16_bf16 v[20:35], v[124:127], v[100:103], v[20:35]
	ds_read_b64_tr_b16 v[124:125], v191 offset:9728
	ds_read_b64_tr_b16 v[126:127], v191 offset:11776
	s_waitcnt lgkmcnt(6)
	v_mfma_f32_32x32x16_bf16 v[20:35], v[128:131], v[104:107], v[20:35]
	ds_read_b64_tr_b16 v[128:129], v191 offset:13824
	ds_read_b64_tr_b16 v[130:131], v191 offset:15872
	s_waitcnt lgkmcnt(6)
	v_mfma_f32_32x32x16_bf16 v[4:19], v[116:119], v[238:241], v[4:19]
	s_waitcnt lgkmcnt(4)
	v_mfma_f32_32x32x16_bf16 v[4:19], v[120:123], v[242:245], v[4:19]
	s_waitcnt lgkmcnt(2)
	v_mfma_f32_32x32x16_bf16 v[4:19], v[124:127], v[100:103], v[4:19]
	s_waitcnt lgkmcnt(0)
	v_mfma_f32_32x32x16_bf16 v[4:19], v[128:131], v[104:107], v[4:19]
	s_setprio 0
	s_branch .Ltail2_a0b0

.LBB0_558:
	s_nop 6
	v_max_f32_e32 v2, v85, v85
	v_max_f32_e32 v100, v84, v84
	v_max_f32_e32 v2, v100, v2
	v_max3_f32 v2, v2, v86, v87
	v_max3_f32 v2, v2, v88, v89
	v_max3_f32 v2, v2, v90, v91
	v_max3_f32 v2, v2, v92, v93
	v_max3_f32 v2, v2, v94, v95
	v_max3_f32 v2, v2, v96, v97
	v_max3_f32 v2, v2, v98, v99
	v_max3_f32 v2, v2, v68, v69
	v_max3_f32 v2, v2, v70, v71
	v_max3_f32 v2, v2, v72, v73
	v_max3_f32 v2, v2, v74, v75
	v_max3_f32 v2, v2, v76, v77
	v_max3_f32 v2, v2, v78, v79
	v_max3_f32 v2, v2, v80, v81
	v_max3_f32 v2, v2, v82, v83
	v_mov_b32_e32 v100, v2
	s_nop 1
	v_permlane32_swap_b32_e32 v2, v100
	v_max_f32_e32 v100, v100, v100
	v_max_f32_e32 v2, v2, v2
	v_max_f32_e32 v100, v2, v100
	s_mov_b32 s15, 0xc2800000
	v_cmp_gt_f32_e32 vcc, s15, v100
	s_mov_b64 s[56:57], -1
	s_nop 0
	v_cndmask_b32_e32 v2, 0, v100, vcc
	v_cndmask_b32_e64 v2, v223, v2, s[8:9]
	v_sub_f32_e32 v101, v100, v2
	v_cmp_ge_f32_e32 vcc, s72, v101
	s_cmp_eq_u64 vcc, exec
	v_max_f32_e32 v101, v2, v2
	v_max_f32_e32 v223, v101, v100
	s_cselect_b64 s[8:9], -1, 0
	v_cndmask_b32_e64 v222, v223, v2, s[8:9]
	v_cmp_eq_f32_e32 vcc, 0, v222
	s_cmp_eq_u64 vcc, exec
	s_cselect_b32 s101, 1, 0
	s_cbranch_scc1 .LBB0_560
	v_sub_f32_e32 v100, v84, v222
	v_exp_f32_e32 v116, v100
	v_sub_f32_e32 v100, v68, v222
	v_sub_f32_e32 v101, v85, v222
	v_exp_f32_e32 v100, v100
	v_exp_f32_e32 v117, v101
	v_sub_f32_e32 v101, v69, v222
	v_sub_f32_e32 v102, v86, v222
	v_exp_f32_e32 v101, v101
	v_exp_f32_e32 v118, v102
	v_sub_f32_e32 v102, v70, v222
	v_exp_f32_e32 v102, v102
	v_add_f32_e32 v103, v100, v116
	v_add_f32_e32 v119, 0, v103
	v_add_f32_e32 v103, v101, v117
	v_pk_add_f32 v[104:105], v[102:103], v[118:119]
	v_sub_f32_e32 v103, v87, v222
	v_pk_add_f32 v[120:121], v[104:105], v[104:105] op_sel_hi:[0,1]
	v_exp_f32_e32 v119, v103
	v_sub_f32_e32 v103, v71, v222
	v_sub_f32_e32 v104, v88, v222
	v_exp_f32_e32 v103, v103
	v_exp_f32_e32 v120, v104
	v_sub_f32_e32 v104, v72, v222
	v_exp_f32_e32 v104, v104
	v_add_f32_e32 v105, v103, v119
	s_mov_b64 s[56:57], 0
	v_pk_add_f32 v[106:107], v[104:105], v[120:121]
	v_sub_f32_e32 v105, v89, v222
	v_pk_add_f32 v[122:123], v[106:107], v[106:107] op_sel_hi:[0,1]
	v_exp_f32_e32 v121, v105
	v_sub_f32_e32 v105, v73, v222
	v_sub_f32_e32 v106, v90, v222
	v_exp_f32_e32 v105, v105
	v_exp_f32_e32 v122, v106
	v_sub_f32_e32 v106, v74, v222
	v_exp_f32_e32 v106, v106
	v_add_f32_e32 v107, v105, v121
	v_pk_add_f32 v[108:109], v[106:107], v[122:123]
	v_sub_f32_e32 v107, v91, v222
	v_pk_add_f32 v[124:125], v[108:109], v[108:109] op_sel_hi:[0,1]
	v_exp_f32_e32 v123, v107
	v_sub_f32_e32 v107, v75, v222
	v_sub_f32_e32 v108, v92, v222
	v_exp_f32_e32 v107, v107
	v_exp_f32_e32 v124, v108
	v_sub_f32_e32 v108, v76, v222
	v_exp_f32_e32 v108, v108
	v_add_f32_e32 v109, v107, v123
	v_pk_add_f32 v[110:111], v[108:109], v[124:125]
	v_sub_f32_e32 v109, v93, v222
	v_pk_add_f32 v[126:127], v[110:111], v[110:111] op_sel_hi:[0,1]
	v_exp_f32_e32 v125, v109
	v_sub_f32_e32 v109, v77, v222
	v_sub_f32_e32 v110, v94, v222
	v_exp_f32_e32 v109, v109
	v_exp_f32_e32 v126, v110
	v_sub_f32_e32 v110, v78, v222
	v_exp_f32_e32 v110, v110
	v_add_f32_e32 v111, v109, v125
	v_pk_add_f32 v[112:113], v[110:111], v[126:127]
	v_sub_f32_e32 v111, v95, v222
	v_pk_add_f32 v[128:129], v[112:113], v[112:113] op_sel_hi:[0,1]
	v_exp_f32_e32 v127, v111
	v_sub_f32_e32 v111, v79, v222
	v_sub_f32_e32 v112, v96, v222
	v_exp_f32_e32 v111, v111
	v_exp_f32_e32 v128, v112
	v_sub_f32_e32 v112, v80, v222
	v_exp_f32_e32 v112, v112
	v_add_f32_e32 v113, v111, v127
	v_pk_add_f32 v[114:115], v[112:113], v[128:129]
	v_sub_f32_e32 v113, v97, v222
	v_pk_add_f32 v[130:131], v[114:115], v[114:115] op_sel_hi:[0,1]
	v_exp_f32_e32 v129, v113
	v_sub_f32_e32 v113, v81, v222
	v_sub_f32_e32 v114, v98, v222
	v_exp_f32_e32 v113, v113
	v_exp_f32_e32 v130, v114
	v_sub_f32_e32 v114, v82, v222
	v_exp_f32_e32 v114, v114
	v_add_f32_e32 v115, v113, v129
	v_pk_add_f32 v[224:225], v[114:115], v[130:131]
	v_sub_f32_e32 v115, v99, v222
	v_exp_f32_e32 v131, v115
	v_add_f32_e32 v224, v224, v225
	v_sub_f32_e32 v115, v83, v222

.LBB0_571:
	s_add_i32 s98, s63, 64
	s_cmp_le_i32 s98, s28
	s_cbranch_scc0 .Lorig_a0b1
	s_setprio 3
	ds_read_b128 v[116:119], v189 offset:24576
	ds_read_b128 v[120:123], v226 offset:24576
	ds_read_b128 v[124:127], v227 offset:24576
	ds_read_b128 v[128:131], v228 offset:24576
	s_waitcnt lgkmcnt(3)
	v_mfma_f32_32x32x16_bf16 v[84:99], v[116:119], v[132:135], 0
	ds_read_b128 v[116:119], v232 offset:24576
	s_waitcnt lgkmcnt(3)
	v_mfma_f32_32x32x16_bf16 v[84:99], v[120:123], v[136:139], v[84:99]
	ds_read_b128 v[120:123], v233 offset:24576
	s_waitcnt lgkmcnt(3)
	v_mfma_f32_32x32x16_bf16 v[84:99], v[124:127], v[140:143], v[84:99]
	ds_read_b128 v[124:127], v234 offset:24576
	s_waitcnt lgkmcnt(3)
	v_mfma_f32_32x32x16_bf16 v[84:99], v[128:131], v[144:147], v[84:99]
	ds_read_b128 v[128:131], v235 offset:24576
	s_waitcnt lgkmcnt(3)
	v_mfma_f32_32x32x16_bf16 v[84:99], v[116:119], v[148:151], v[84:99]
	ds_read_b128 v[116:119], v190 offset:24576
	s_waitcnt lgkmcnt(3)
	v_mfma_f32_32x32x16_bf16 v[84:99], v[120:123], v[152:155], v[84:99]
	ds_read_b128 v[120:123], v229 offset:24576
	s_waitcnt lgkmcnt(3)
	v_mfma_f32_32x32x16_bf16 v[84:99], v[124:127], v[156:159], v[84:99]
	ds_read_b128 v[124:127], v230 offset:24576
	s_waitcnt lgkmcnt(3)
	v_mfma_f32_32x32x16_bf16 v[84:99], v[128:131], v[160:163], v[84:99]
	ds_read_b128 v[128:131], v231 offset:24576
	s_waitcnt lgkmcnt(3)
	v_mfma_f32_32x32x16_bf16 v[84:99], v[116:119], v[164:167], v[84:99]
	ds_read_b128 v[116:119], v189 offset:32768
	s_waitcnt lgkmcnt(3)
	v_mfma_f32_32x32x16_bf16 v[84:99], v[120:123], v[172:175], v[84:99]
	ds_read_b128 v[120:123], v226 offset:32768
	s_waitcnt lgkmcnt(3)
	v_mfma_f32_32x32x16_bf16 v[84:99], v[124:127], v[168:171], v[84:99]
	ds_read_b128 v[124:127], v227 offset:32768
	s_waitcnt lgkmcnt(3)
	v_mfma_f32_32x32x16_bf16 v[84:99], v[128:131], v[176:179], v[84:99]
	ds_read_b128 v[128:131], v228 offset:32768
	s_waitcnt lgkmcnt(3)
	v_mfma_f32_32x32x16_bf16 v[68:83], v[116:119], v[132:135], 0
	ds_read_b128 v[116:119], v232 offset:32768
	s_waitcnt lgkmcnt(3)
	v_mfma_f32_32x32x16_bf16 v[68:83], v[120:123], v[136:139], v[68:83]
	ds_read_b128 v[120:123], v233 offset:32768
	s_waitcnt lgkmcnt(3)
	v_mfma_f32_32x32x16_bf16 v[68:83], v[124:127], v[140:143], v[68:83]
	ds_read_b128 v[124:127], v234 offset:32768
	s_waitcnt lgkmcnt(3)
	v_mfma_f32_32x32x16_bf16 v[68:83], v[128:131], v[144:147], v[68:83]
	ds_read_b128 v[128:131], v235 offset:32768
	s_waitcnt lgkmcnt(3)
	v_mfma_f32_32x32x16_bf16 v[68:83], v[116:119], v[148:151], v[68:83]
	ds_read_b128 v[116:119], v190 offset:28672
	s_waitcnt lgkmcnt(3)
	v_mfma_f32_32x32x16_bf16 v[68:83], v[120:123], v[152:155], v[68:83]
	ds_read_b128 v[120:123], v229 offset:28672
	s_waitcnt lgkmcnt(3)
	v_mfma_f32_32x32x16_bf16 v[68:83], v[124:127], v[156:159], v[68:83]
	ds_read_b128 v[124:127], v230 offset:28672
	s_waitcnt lgkmcnt(3)
	v_mfma_f32_32x32x16_bf16 v[68:83], v[128:131], v[160:163], v[68:83]
	ds_read_b128 v[128:131], v231 offset:28672
	s_waitcnt lgkmcnt(3)
	v_mfma_f32_32x32x16_bf16 v[68:83], v[116:119], v[164:167], v[68:83]
	s_waitcnt lgkmcnt(2)
	v_mfma_f32_32x32x16_bf16 v[68:83], v[120:123], v[172:175], v[68:83]
	s_waitcnt lgkmcnt(1)
	v_mfma_f32_32x32x16_bf16 v[68:83], v[124:127], v[168:171], v[68:83]
	s_waitcnt lgkmcnt(0)
	v_mfma_f32_32x32x16_bf16 v[68:83], v[128:131], v[176:179], v[68:83]
	ds_read_b64_tr_b16 v[116:117], v191 offset:16384
	ds_read_b64_tr_b16 v[118:119], v191 offset:18432
	ds_read_b64_tr_b16 v[120:121], v191 offset:20480
	ds_read_b64_tr_b16 v[122:123], v191 offset:22528
	ds_read_b64_tr_b16 v[124:125], v191 offset:24576
	ds_read_b64_tr_b16 v[126:127], v191 offset:26624
	ds_read_b64_tr_b16 v[128:129], v191 offset:28672
	ds_read_b64_tr_b16 v[130:131], v191 offset:30720
	s_setprio 0
	s_nop 2
	s_cmp_eq_u32 s101, 1
	s_cbranch_scc0 .Lsub_a0b1
	v_exp_f32_e32 v100, v84
	v_exp_f32_e32 v101, v85
	v_exp_f32_e32 v102, v86
	v_exp_f32_e32 v103, v87
	v_exp_f32_e32 v104, v88
	v_exp_f32_e32 v105, v89
	v_exp_f32_e32 v106, v90
	v_exp_f32_e32 v107, v91
	v_exp_f32_e32 v108, v92
	v_exp_f32_e32 v109, v93
	v_exp_f32_e32 v110, v94
	v_exp_f32_e32 v111, v95
	v_exp_f32_e32 v112, v96
	v_exp_f32_e32 v113, v97
	v_exp_f32_e32 v114, v98
	v_exp_f32_e32 v115, v99
	v_add_f32_e32 v237, v100, v101
	v_add_f32_e32 v251, v102, v103
	v_add_f32_e32 v237, v237, v104
	v_add_f32_e32 v251, v251, v105
	v_add_f32_e32 v237, v237, v106
	v_add_f32_e32 v251, v251, v107
	v_add_f32_e32 v237, v237, v108
	v_add_f32_e32 v251, v251, v109
	v_add_f32_e32 v237, v237, v110
	v_add_f32_e32 v251, v251, v111
	v_add_f32_e32 v237, v237, v112
	v_add_f32_e32 v251, v251, v113
	v_add_f32_e32 v237, v237, v114
	v_add_f32_e32 v251, v251, v115
	v_add_f32_e32 v237, v237, v251
	v_cvt_pk_bf16_f32 v238, v100, v101
	v_cvt_pk_bf16_f32 v239, v102, v103
	v_cvt_pk_bf16_f32 v240, v104, v105
	v_cvt_pk_bf16_f32 v241, v106, v107
	v_cvt_pk_bf16_f32 v242, v108, v109
	v_cvt_pk_bf16_f32 v243, v110, v111
	v_cvt_pk_bf16_f32 v244, v112, v113
	v_cvt_pk_bf16_f32 v245, v114, v115
	s_nop 1
	v_permlane32_swap_b32_e32 v238, v240
	v_permlane32_swap_b32_e32 v239, v241
	v_permlane32_swap_b32_e32 v242, v244
	v_permlane32_swap_b32_e32 v243, v245
	v_exp_f32_e32 v100, v68
	v_exp_f32_e32 v101, v69
	v_exp_f32_e32 v102, v70
	v_exp_f32_e32 v103, v71
	v_exp_f32_e32 v104, v72
	v_exp_f32_e32 v105, v73
	v_exp_f32_e32 v106, v74
	v_exp_f32_e32 v107, v75
	v_exp_f32_e32 v108, v76
	v_exp_f32_e32 v109, v77
	v_exp_f32_e32 v110, v78
	v_exp_f32_e32 v111, v79
	v_exp_f32_e32 v112, v80
	v_exp_f32_e32 v113, v81
	v_exp_f32_e32 v114, v82
	v_exp_f32_e32 v115, v83
	v_add_f32_e32 v250, v100, v101
	v_add_f32_e32 v251, v102, v103
	v_add_f32_e32 v250, v250, v104
	v_add_f32_e32 v251, v251, v105
	v_add_f32_e32 v250, v250, v106
	v_add_f32_e32 v251, v251, v107
	v_add_f32_e32 v250, v250, v108
	v_add_f32_e32 v251, v251, v109
	v_add_f32_e32 v250, v250, v110
	v_add_f32_e32 v251, v251, v111
	v_add_f32_e32 v250, v250, v112
	v_add_f32_e32 v251, v251, v113
	v_add_f32_e32 v250, v250, v114
	v_add_f32_e32 v251, v251, v115
	v_add_f32_e32 v250, v250, v251
	v_cvt_pk_bf16_f32 v100, v100, v101
	v_cvt_pk_bf16_f32 v101, v102, v103
	v_cvt_pk_bf16_f32 v102, v104, v105
	v_cvt_pk_bf16_f32 v103, v106, v107
	v_cvt_pk_bf16_f32 v104, v108, v109
	v_cvt_pk_bf16_f32 v105, v110, v111
	v_cvt_pk_bf16_f32 v106, v112, v113
	v_cvt_pk_bf16_f32 v107, v114, v115
	s_nop 1
	v_permlane32_swap_b32_e32 v100, v102
	v_permlane32_swap_b32_e32 v101, v103
	v_permlane32_swap_b32_e32 v104, v106
	v_permlane32_swap_b32_e32 v105, v107
	s_branch .Lsum_a0b1

.Lsum_a0b1:
	v_add_f32_e32 v237, v237, v250
	v_cmp_gt_f32_e32 vcc, 0x5f800000, v237
	v_mov_b32_e32 v250, v237
	s_nop 1
	v_permlane32_swap_b32_e32 v237, v250
	v_add_f32_e32 v237, v237, v250
	s_cmp_eq_u64 vcc, exec
	s_cbranch_scc0 .Lfb_a0b1
	v_add_f32_e32 v221, v237, v221
	v_mov_b32_e32 v223, v222
	s_setprio 3
	s_waitcnt lgkmcnt(6)
	v_mfma_f32_32x32x16_bf16 v[52:67], v[116:119], v[238:241], v[52:67]
	ds_read_b64_tr_b16 v[116:117], v191 offset:16896
	ds_read_b64_tr_b16 v[118:119], v191 offset:18944
	s_waitcnt lgkmcnt(6)
	v_mfma_f32_32x32x16_bf16 v[52:67], v[120:123], v[242:245], v[52:67]
	ds_read_b64_tr_b16 v[120:121], v191 offset:20992
	ds_read_b64_tr_b16 v[122:123], v191 offset:23040
	s_waitcnt lgkmcnt(6)
	v_mfma_f32_32x32x16_bf16 v[52:67], v[124:127], v[100:103], v[52:67]
	ds_read_b64_tr_b16 v[124:125], v191 offset:25088
	ds_read_b64_tr_b16 v[126:127], v191 offset:27136
	s_waitcnt lgkmcnt(6)
	v_mfma_f32_32x32x16_bf16 v[52:67], v[128:131], v[104:107], v[52:67]
	ds_read_b64_tr_b16 v[128:129], v191 offset:29184
	ds_read_b64_tr_b16 v[130:131], v191 offset:31232
	s_waitcnt lgkmcnt(6)
	v_mfma_f32_32x32x16_bf16 v[36:51], v[116:119], v[238:241], v[36:51]
	ds_read_b64_tr_b16 v[116:117], v191 offset:17408
	ds_read_b64_tr_b16 v[118:119], v191 offset:19456
	s_waitcnt lgkmcnt(6)
	v_mfma_f32_32x32x16_bf16 v[36:51], v[120:123], v[242:245], v[36:51]
	ds_read_b64_tr_b16 v[120:121], v191 offset:21504
	ds_read_b64_tr_b16 v[122:123], v191 offset:23552
	s_waitcnt lgkmcnt(6)
	v_mfma_f32_32x32x16_bf16 v[36:51], v[124:127], v[100:103], v[36:51]
	ds_read_b64_tr_b16 v[124:125], v191 offset:25600
	ds_read_b64_tr_b16 v[126:127], v191 offset:27648
	s_waitcnt lgkmcnt(6)
	v_mfma_f32_32x32x16_bf16 v[36:51], v[128:131], v[104:107], v[36:51]
	ds_read_b64_tr_b16 v[128:129], v191 offset:29696
	ds_read_b64_tr_b16 v[130:131], v191 offset:31744
	s_waitcnt lgkmcnt(6)
	v_mfma_f32_32x32x16_bf16 v[20:35], v[116:119], v[238:241], v[20:35]
	ds_read_b64_tr_b16 v[116:117], v191 offset:17920
	ds_read_b64_tr_b16 v[118:119], v191 offset:19968
	s_waitcnt lgkmcnt(6)
	v_mfma_f32_32x32x16_bf16 v[20:35], v[120:123], v[242:245], v[20:35]
	ds_read_b64_tr_b16 v[120:121], v191 offset:22016
	ds_read_b64_tr_b16 v[122:123], v191 offset:24064
	s_waitcnt lgkmcnt(6)
	v_mfma_f32_32x32x16_bf16 v[20:35], v[124:127], v[100:103], v[20:35]
	ds_read_b64_tr_b16 v[124:125], v191 offset:26112
	ds_read_b64_tr_b16 v[126:127], v191 offset:28160
	s_waitcnt lgkmcnt(6)
	v_mfma_f32_32x32x16_bf16 v[20:35], v[128:131], v[104:107], v[20:35]
	ds_read_b64_tr_b16 v[128:129], v191 offset:30208
	ds_read_b64_tr_b16 v[130:131], v191 offset:32256
	s_waitcnt lgkmcnt(6)
	v_mfma_f32_32x32x16_bf16 v[4:19], v[116:119], v[238:241], v[4:19]
	s_waitcnt lgkmcnt(4)
	v_mfma_f32_32x32x16_bf16 v[4:19], v[120:123], v[242:245], v[4:19]
	s_waitcnt lgkmcnt(2)
	v_mfma_f32_32x32x16_bf16 v[4:19], v[124:127], v[100:103], v[4:19]
	s_waitcnt lgkmcnt(0)
	v_mfma_f32_32x32x16_bf16 v[4:19], v[128:131], v[104:107], v[4:19]
	s_setprio 0
	s_branch .Ltail2_a0b1

.LBB0_573:
	s_nop 5
	v_max_f32_e32 v2, v85, v85
	v_max_f32_e32 v100, v84, v84
	v_max_f32_e32 v2, v100, v2
	v_max3_f32 v2, v2, v86, v87
	v_max3_f32 v2, v2, v88, v89
	v_max3_f32 v2, v2, v90, v91
	v_max3_f32 v2, v2, v92, v93
	v_max3_f32 v2, v2, v94, v95
	v_max3_f32 v2, v2, v96, v97
	v_max3_f32 v2, v2, v98, v99
	v_max3_f32 v2, v2, v68, v69
	v_max3_f32 v2, v2, v70, v71
	v_max3_f32 v2, v2, v72, v73
	v_max3_f32 v2, v2, v74, v75
	v_max3_f32 v2, v2, v76, v77
	v_max3_f32 v2, v2, v78, v79
	v_max3_f32 v2, v2, v80, v81
	v_max3_f32 v2, v2, v82, v83
	v_mov_b32_e32 v100, v2
	s_nop 1
	v_permlane32_swap_b32_e32 v2, v100
	v_max_f32_e32 v100, v100, v100
	v_max_f32_e32 v2, v2, v2
	v_max_f32_e32 v2, v2, v100
	v_sub_f32_e32 v100, v2, v222
	v_cmp_ge_f32_e32 vcc, s72, v100
	s_cmp_eq_u64 vcc, exec
	v_max_f32_e32 v100, v222, v222
	v_max_f32_e32 v2, v100, v2
	s_cselect_b64 s[6:7], -1, 0
	v_cndmask_b32_e64 v223, v2, v222, s[6:7]
	v_cmp_eq_f32_e32 vcc, 0, v223
	s_cmp_eq_u64 vcc, exec
	s_cselect_b32 s101, 1, 0
	s_mov_b64 s[56:57], -1
	s_cbranch_scc1 .LBB0_575
	v_sub_f32_e32 v100, v84, v223
	v_exp_f32_e32 v116, v100
	v_sub_f32_e32 v100, v68, v223
	v_sub_f32_e32 v101, v85, v223
	v_exp_f32_e32 v100, v100
	v_exp_f32_e32 v117, v101
	v_sub_f32_e32 v101, v69, v223
	v_sub_f32_e32 v102, v86, v223
	v_exp_f32_e32 v101, v101
	v_exp_f32_e32 v118, v102
	v_sub_f32_e32 v102, v70, v223
	v_exp_f32_e32 v102, v102
	v_add_f32_e32 v103, v100, v116
	v_add_f32_e32 v119, 0, v103
	v_add_f32_e32 v103, v101, v117
	v_pk_add_f32 v[104:105], v[102:103], v[118:119]
	v_sub_f32_e32 v103, v87, v223
	v_pk_add_f32 v[120:121], v[104:105], v[104:105] op_sel_hi:[0,1]
	v_exp_f32_e32 v119, v103
	v_sub_f32_e32 v103, v71, v223
	v_sub_f32_e32 v104, v88, v223
	v_exp_f32_e32 v103, v103
	v_exp_f32_e32 v120, v104
	v_sub_f32_e32 v104, v72, v223
	v_exp_f32_e32 v104, v104
	v_add_f32_e32 v105, v103, v119
	s_mov_b64 s[56:57], 0
	v_pk_add_f32 v[106:107], v[104:105], v[120:121]
	v_sub_f32_e32 v105, v89, v223
	v_pk_add_f32 v[122:123], v[106:107], v[106:107] op_sel_hi:[0,1]
	v_exp_f32_e32 v121, v105
	v_sub_f32_e32 v105, v73, v223
	v_sub_f32_e32 v106, v90, v223
	v_exp_f32_e32 v105, v105
	v_exp_f32_e32 v122, v106
	v_sub_f32_e32 v106, v74, v223
	v_exp_f32_e32 v106, v106
	v_add_f32_e32 v107, v105, v121
	v_pk_add_f32 v[108:109], v[106:107], v[122:123]
	v_sub_f32_e32 v107, v91, v223
	v_pk_add_f32 v[124:125], v[108:109], v[108:109] op_sel_hi:[0,1]
	v_exp_f32_e32 v123, v107
	v_sub_f32_e32 v107, v75, v223
	v_sub_f32_e32 v108, v92, v223
	v_exp_f32_e32 v107, v107
	v_exp_f32_e32 v124, v108
	v_sub_f32_e32 v108, v76, v223
	v_exp_f32_e32 v108, v108
	v_add_f32_e32 v109, v107, v123
	v_pk_add_f32 v[110:111], v[108:109], v[124:125]
	v_sub_f32_e32 v109, v93, v223
	v_pk_add_f32 v[126:127], v[110:111], v[110:111] op_sel_hi:[0,1]
	v_exp_f32_e32 v125, v109
	v_sub_f32_e32 v109, v77, v223
	v_sub_f32_e32 v110, v94, v223
	v_exp_f32_e32 v109, v109
	v_exp_f32_e32 v126, v110
	v_sub_f32_e32 v110, v78, v223
	v_exp_f32_e32 v110, v110
	v_add_f32_e32 v111, v109, v125
	v_pk_add_f32 v[112:113], v[110:111], v[126:127]
	v_sub_f32_e32 v111, v95, v223
	v_pk_add_f32 v[128:129], v[112:113], v[112:113] op_sel_hi:[0,1]
	v_exp_f32_e32 v127, v111
	v_sub_f32_e32 v111, v79, v223
	v_sub_f32_e32 v112, v96, v223
	v_exp_f32_e32 v111, v111
	v_exp_f32_e32 v128, v112
	v_sub_f32_e32 v112, v80, v223
	v_exp_f32_e32 v112, v112
	v_add_f32_e32 v113, v111, v127
	v_pk_add_f32 v[114:115], v[112:113], v[128:129]
	v_sub_f32_e32 v113, v97, v223
	v_pk_add_f32 v[130:131], v[114:115], v[114:115] op_sel_hi:[0,1]
	v_exp_f32_e32 v129, v113
	v_sub_f32_e32 v113, v81, v223
	v_sub_f32_e32 v114, v98, v223
	v_exp_f32_e32 v113, v113
	v_exp_f32_e32 v130, v114
	v_sub_f32_e32 v114, v82, v223
	v_exp_f32_e32 v114, v114
	v_add_f32_e32 v115, v113, v129
	v_pk_add_f32 v[224:225], v[114:115], v[130:131]
	v_sub_f32_e32 v115, v99, v223
	v_exp_f32_e32 v131, v115
	v_add_f32_e32 v224, v224, v225
	v_sub_f32_e32 v115, v83, v223

; template <int layer>
; __device__ __forceinline__ void attn_phase(LAS unsigned char* lds) {
;     ...
;             float m_reg = 0.f, l_reg = 0.f; f32x16 o[4];
; #pragma unroll
;             for (int d0 = 0; d0 < 4; ++d0)
; #pragma unroll
;                 for (int r = 0; r < 16; ++r) o[d0][r] = 0.f;
;     ...
;             FA_ISSUE(0, 0);
;             for (int t = 0; t < NT; t += 2) { FA_STEP(t, 0); FA_STEP(t + 1, 1); }
.LBB0_1425:
	v_mov_b32_e32 v16, v3
	v_mov_b32_e32 v17, v3
	v_mov_b32_e32 v2, v3
	v_mov_b32_e32 v4, v3
	v_mov_b32_e32 v5, v3
	v_mov_b32_e32 v6, v3
	v_mov_b32_e32 v7, v3
	v_mov_b32_e32 v8, v3
	v_mov_b32_e32 v9, v3
	v_mov_b32_e32 v10, v3
	v_mov_b32_e32 v11, v3
	v_mov_b32_e32 v12, v3
	v_mov_b32_e32 v13, v3
	v_mov_b32_e32 v14, v3
	v_mov_b32_e32 v15, v3
	v_mov_b64_e32 v[66:67], v[16:17]
	v_mov_b64_e32 v[50:51], v[16:17]
	v_mov_b64_e32 v[34:35], v[16:17]
	s_lshr_b32 s41, s10, 6
	v_readlane_b32 s54, v252, 19
	v_readlane_b32 s56, v252, 35
	v_mov_b64_e32 v[64:65], v[14:15]
	v_mov_b64_e32 v[62:63], v[12:13]
	v_mov_b64_e32 v[60:61], v[10:11]
	v_mov_b64_e32 v[58:59], v[8:9]
	v_mov_b64_e32 v[56:57], v[6:7]
	v_mov_b64_e32 v[54:55], v[4:5]
	v_mov_b64_e32 v[52:53], v[2:3]
	v_mov_b64_e32 v[48:49], v[14:15]
	v_mov_b64_e32 v[46:47], v[12:13]
	v_mov_b64_e32 v[44:45], v[10:11]
	v_mov_b64_e32 v[42:43], v[8:9]
	v_mov_b64_e32 v[40:41], v[6:7]
	v_mov_b64_e32 v[38:39], v[4:5]
	v_mov_b64_e32 v[36:37], v[2:3]
	v_mov_b64_e32 v[32:33], v[14:15]
	v_mov_b64_e32 v[30:31], v[12:13]
	v_mov_b64_e32 v[28:29], v[10:11]
	v_mov_b64_e32 v[26:27], v[8:9]
	v_mov_b64_e32 v[24:25], v[6:7]
	v_mov_b64_e32 v[22:23], v[4:5]
	v_mov_b64_e32 v[20:21], v[2:3]
	v_mov_b64_e32 v[18:19], v[16:17]
	s_xor_b64 s[50:51], s[8:9], -1
	s_add_i32 s41, s41, 4
	s_or_b32 s75, s40, 31
	v_add_u32_e32 v190, s10, v184
	s_mov_b32 s71, 0
	v_mov_b32_e32 v193, 0
	s_mov_b32 s101, 1
	s_mov_b32 s18, 63
	s_mov_b64 s[52:53], s[48:49]
	v_readlane_b32 s55, v252, 20
	v_readlane_b32 s57, v252, 36
	v_mov_b64_e32 v[16:17], v[14:15]
	v_mov_b64_e32 v[14:15], v[12:13]
	v_mov_b64_e32 v[12:13], v[10:11]
	v_mov_b64_e32 v[10:11], v[8:9]
	v_mov_b64_e32 v[8:9], v[6:7]
	v_mov_b64_e32 v[6:7], v[4:5]
	v_mov_b64_e32 v[4:5], v[2:3]
	v_mov_b32_e32 v191, 0
	s_mov_b32 s19, 0
	s_branch .LBB0_1428

.LBB0_1430:
	s_or_b32 s8, s19, 1
	s_cmp_ge_u32 s8, s41
	s_waitcnt lgkmcnt(0)
	s_barrier
	s_cselect_b64 s[8:9], -1, 0
	s_xor_b64 s[58:59], s[20:21], -1
	s_or_b64 s[8:9], s[58:59], s[8:9]
	s_and_b64 vcc, exec, s[8:9]
	s_cbranch_vccnz .LBB0_1433
	s_add_u32 s8, s54, 0xfff00000
	s_addc_u32 s9, s55, -1
	s_mov_b32 m0, s79
	s_nop 0
	global_load_lds_dwordx4 v1, s[8:9]
	s_mov_b32 m0, s89
	s_nop 0
	global_load_lds_dwordx4 v178, s[8:9]
	s_mov_b32 m0, s90
	s_nop 0
	global_load_lds_dwordx4 v179, s[8:9]
	s_mov_b32 m0, s91
	s_nop 0
	global_load_lds_dwordx4 v180, s[8:9]
	s_add_u32 s8, s56, 0xfff00000
	s_addc_u32 s9, s57, -1
	s_mov_b32 m0, s80
	s_nop 0
	global_load_lds_dwordx4 v133, s[8:9]
	s_and_b64 vcc, exec, s[6:7]
	s_mov_b32 m0, s92
	s_nop 0
	global_load_lds_dwordx4 v181, s[8:9]
	s_mov_b32 m0, s93
	s_nop 0
	global_load_lds_dwordx4 v182, s[8:9]
	s_mov_b32 m0, s94
	s_nop 0
	global_load_lds_dwordx4 v183, s[8:9]
	s_cbranch_vccnz .LBB0_1433
	s_add_u32 s8, s52, 0xffffff00
	s_addc_u32 s9, s53, -1
	s_mov_b32 m0, s83
	s_nop 0
	global_load_lds_dword v175, s[8:9]

.LBB0_1439:
	s_add_i32 s19, s19, 2
	s_cmp_ge_u32 s19, s41
	s_cselect_b64 s[10:11], -1, 0
	s_cmp_lt_u32 s19, s41
	s_waitcnt lgkmcnt(0)
	s_barrier
	s_cselect_b64 s[42:43], -1, 0
	s_and_b64 s[42:43], s[20:21], s[42:43]
	s_andn2_b64 vcc, exec, s[42:43]
	s_cbranch_vccnz .LBB0_1442
	s_mov_b32 m0, s77
	s_nop 0
	global_load_lds_dwordx4 v1, s[54:55]
	s_and_b64 vcc, exec, s[6:7]
	s_mov_b32 m0, s84
	s_nop 0
	global_load_lds_dwordx4 v178, s[54:55]
	s_mov_b32 m0, s85
	s_nop 0
	global_load_lds_dwordx4 v179, s[54:55]
	s_mov_b32 m0, s86
	s_nop 0
	global_load_lds_dwordx4 v180, s[54:55]
	s_mov_b32 m0, s78
	s_nop 0
	global_load_lds_dwordx4 v133, s[56:57]
	s_mov_b32 m0, s76
	s_nop 0
	global_load_lds_dwordx4 v181, s[56:57]
	s_mov_b32 m0, s87
	s_nop 0
	global_load_lds_dwordx4 v182, s[56:57]
	s_mov_b32 m0, s88
	s_nop 0
	global_load_lds_dwordx4 v183, s[56:57]
	s_cbranch_vccnz .LBB0_1442
	s_mov_b32 m0, s81
	s_nop 0
	global_load_lds_dword v175, s[52:53]

.LBB0_1452:
	s_cmp_le_i32 s18, s40
	s_cbranch_scc0 .Lorig_a1b0
	s_cmp_eq_u32 s71, 0
	s_cbranch_scc1 .Lorig_a1b0
	s_setprio 3
	ds_read_b128 v[140:143], v176
	ds_read_b128 v[144:147], v176 offset:32
	ds_read_b128 v[148:151], v176 offset:64
	ds_read_b128 v[152:155], v176 offset:96
	ds_read_b128 v[208:211], v172 offset:32768
	ds_read_b128 v[212:215], v206 offset:32768
	ds_read_b128 v[216:219], v207 offset:32768
	ds_read_b128 v[220:223], v237 offset:32768
	ds_read_b128 v[224:227], v244 offset:32768
	ds_read_b128 v[228:231], v245 offset:32768
	ds_read_b128 v[232:235], v246 offset:32768
	ds_read_b128 v[238:241], v247 offset:32768
	ds_read_b128 v[156:159], v176 offset:128
	ds_read_b128 v[160:163], v176 offset:160
	ds_read_b128 v[164:167], v176 offset:192
	ds_read_b128 v[168:171], v176 offset:224
	s_waitcnt lgkmcnt(11)
	v_mfma_f32_32x32x16_bf16 v[84:99], v[208:211], v[100:103], v[140:155]
	ds_read_b128 v[208:211], v172 offset:40960
	s_waitcnt lgkmcnt(11)
	v_mfma_f32_32x32x16_bf16 v[84:99], v[212:215], v[104:107], v[84:99]
	ds_read_b128 v[212:215], v206 offset:40960
	s_waitcnt lgkmcnt(11)
	v_mfma_f32_32x32x16_bf16 v[84:99], v[216:219], v[108:111], v[84:99]
	ds_read_b128 v[216:219], v207 offset:40960
	s_waitcnt lgkmcnt(11)
	v_mfma_f32_32x32x16_bf16 v[84:99], v[220:223], v[112:115], v[84:99]
	ds_read_b128 v[220:223], v237 offset:40960
	s_waitcnt lgkmcnt(11)
	v_mfma_f32_32x32x16_bf16 v[84:99], v[224:227], v[116:119], v[84:99]
	ds_read_b128 v[224:227], v244 offset:40960
	s_waitcnt lgkmcnt(11)
	v_mfma_f32_32x32x16_bf16 v[84:99], v[228:231], v[120:123], v[84:99]
	ds_read_b128 v[228:231], v245 offset:40960
	s_waitcnt lgkmcnt(11)
	v_mfma_f32_32x32x16_bf16 v[84:99], v[232:235], v[124:127], v[84:99]
	ds_read_b128 v[232:235], v246 offset:40960
	s_waitcnt lgkmcnt(11)
	v_mfma_f32_32x32x16_bf16 v[84:99], v[238:241], v[128:131], v[84:99]
	ds_read_b128 v[238:241], v247 offset:40960
	s_waitcnt lgkmcnt(7)
	v_mfma_f32_32x32x16_bf16 v[68:83], v[208:211], v[100:103], v[156:171]
	s_waitcnt lgkmcnt(6)
	v_mfma_f32_32x32x16_bf16 v[68:83], v[212:215], v[104:107], v[68:83]
	s_waitcnt lgkmcnt(5)
	v_mfma_f32_32x32x16_bf16 v[68:83], v[216:219], v[108:111], v[68:83]
	s_waitcnt lgkmcnt(4)
	v_mfma_f32_32x32x16_bf16 v[68:83], v[220:223], v[112:115], v[68:83]
	s_waitcnt lgkmcnt(3)
	v_mfma_f32_32x32x16_bf16 v[68:83], v[224:227], v[116:119], v[68:83]
	s_waitcnt lgkmcnt(2)
	v_mfma_f32_32x32x16_bf16 v[68:83], v[228:231], v[120:123], v[68:83]
	s_waitcnt lgkmcnt(1)
	v_mfma_f32_32x32x16_bf16 v[68:83], v[232:235], v[124:127], v[68:83]
	s_waitcnt lgkmcnt(0)
	v_mfma_f32_32x32x16_bf16 v[68:83], v[238:241], v[128:131], v[68:83]
	ds_read_b64_tr_b16 v[208:209], v174 offset:0
	ds_read_b64_tr_b16 v[210:211], v174 offset:2048
	ds_read_b64_tr_b16 v[212:213], v174 offset:4096
	ds_read_b64_tr_b16 v[214:215], v174 offset:6144
	ds_read_b64_tr_b16 v[216:217], v174 offset:8192
	ds_read_b64_tr_b16 v[218:219], v174 offset:10240
	ds_read_b64_tr_b16 v[220:221], v174 offset:12288
	ds_read_b64_tr_b16 v[222:223], v174 offset:14336
	s_setprio 0
	s_nop 2
	s_cmp_eq_u32 s101, 1
	s_cbranch_scc0 .Lsub_a1b0
	v_exp_f32_e32 v140, v84
	v_exp_f32_e32 v141, v85
	v_exp_f32_e32 v142, v86
	v_exp_f32_e32 v143, v87
	v_exp_f32_e32 v144, v88
	v_exp_f32_e32 v145, v89
	v_exp_f32_e32 v146, v90
	v_exp_f32_e32 v147, v91
	v_exp_f32_e32 v148, v92
	v_exp_f32_e32 v149, v93
	v_exp_f32_e32 v150, v94
	v_exp_f32_e32 v151, v95
	v_exp_f32_e32 v152, v96
	v_exp_f32_e32 v153, v97
	v_exp_f32_e32 v154, v98
	v_exp_f32_e32 v155, v99
	v_add_f32_e32 v248, v140, v141
	v_add_f32_e32 v250, v142, v143
	v_add_f32_e32 v248, v248, v144
	v_add_f32_e32 v250, v250, v145
	v_add_f32_e32 v248, v248, v146
	v_add_f32_e32 v250, v250, v147
	v_add_f32_e32 v248, v248, v148
	v_add_f32_e32 v250, v250, v149
	v_add_f32_e32 v248, v248, v150
	v_add_f32_e32 v250, v250, v151
	v_add_f32_e32 v248, v248, v152
	v_add_f32_e32 v250, v250, v153
	v_add_f32_e32 v248, v248, v154
	v_add_f32_e32 v250, v250, v155
	v_add_f32_e32 v248, v248, v250
	v_cvt_pk_bf16_f32 v140, v140, v141
	v_cvt_pk_bf16_f32 v141, v142, v143
	v_cvt_pk_bf16_f32 v142, v144, v145
	v_cvt_pk_bf16_f32 v143, v146, v147
	v_cvt_pk_bf16_f32 v144, v148, v149
	v_cvt_pk_bf16_f32 v145, v150, v151
	v_cvt_pk_bf16_f32 v146, v152, v153
	v_cvt_pk_bf16_f32 v147, v154, v155
	s_nop 1
	v_permlane32_swap_b32_e32 v140, v142
	v_permlane32_swap_b32_e32 v141, v143
	v_permlane32_swap_b32_e32 v144, v146
	v_permlane32_swap_b32_e32 v145, v147
	v_exp_f32_e32 v156, v68
	v_exp_f32_e32 v157, v69
	v_exp_f32_e32 v158, v70
	v_exp_f32_e32 v159, v71
	v_exp_f32_e32 v160, v72
	v_exp_f32_e32 v161, v73
	v_exp_f32_e32 v162, v74
	v_exp_f32_e32 v163, v75
	v_exp_f32_e32 v164, v76
	v_exp_f32_e32 v165, v77
	v_exp_f32_e32 v166, v78
	v_exp_f32_e32 v167, v79
	v_exp_f32_e32 v168, v80
	v_exp_f32_e32 v169, v81
	v_exp_f32_e32 v170, v82
	v_exp_f32_e32 v171, v83
	v_add_f32_e32 v249, v156, v157
	v_add_f32_e32 v250, v158, v159
	v_add_f32_e32 v249, v249, v160
	v_add_f32_e32 v250, v250, v161
	v_add_f32_e32 v249, v249, v162
	v_add_f32_e32 v250, v250, v163
	v_add_f32_e32 v249, v249, v164
	v_add_f32_e32 v250, v250, v165
	v_add_f32_e32 v249, v249, v166
	v_add_f32_e32 v250, v250, v167
	v_add_f32_e32 v249, v249, v168
	v_add_f32_e32 v250, v250, v169
	v_add_f32_e32 v249, v249, v170
	v_add_f32_e32 v250, v250, v171
	v_add_f32_e32 v249, v249, v250
	v_cvt_pk_bf16_f32 v156, v156, v157
	v_cvt_pk_bf16_f32 v157, v158, v159
	v_cvt_pk_bf16_f32 v158, v160, v161
	v_cvt_pk_bf16_f32 v159, v162, v163
	v_cvt_pk_bf16_f32 v160, v164, v165
	v_cvt_pk_bf16_f32 v161, v166, v167
	v_cvt_pk_bf16_f32 v162, v168, v169
	v_cvt_pk_bf16_f32 v163, v170, v171
	s_nop 1
	v_permlane32_swap_b32_e32 v156, v158
	v_permlane32_swap_b32_e32 v157, v159
	v_permlane32_swap_b32_e32 v160, v162
	v_permlane32_swap_b32_e32 v161, v163
	s_branch .Lsum_a1b0

.Lsum_a1b0:
	v_add_f32_e32 v248, v248, v249
	v_cmp_gt_f32_e32 vcc, 0x5f800000, v248
	v_mov_b32_e32 v249, v248
	s_nop 1
	v_permlane32_swap_b32_e32 v248, v249
	v_add_f32_e32 v248, v248, v249
	s_cmp_eq_u64 vcc, exec
	s_cbranch_scc0 .Lfb_a1b0
	v_add_f32_e32 v191, v248, v191
	v_mov_b32_e32 v192, v193
	s_setprio 3
	s_waitcnt lgkmcnt(6)
	v_mfma_f32_32x32x16_bf16 v[52:67], v[208:211], v[140:143], v[52:67]
	ds_read_b64_tr_b16 v[208:209], v174 offset:512
	ds_read_b64_tr_b16 v[210:211], v174 offset:2560
	s_waitcnt lgkmcnt(6)
	v_mfma_f32_32x32x16_bf16 v[52:67], v[212:215], v[144:147], v[52:67]
	ds_read_b64_tr_b16 v[212:213], v174 offset:4608
	ds_read_b64_tr_b16 v[214:215], v174 offset:6656
	s_waitcnt lgkmcnt(6)
	v_mfma_f32_32x32x16_bf16 v[52:67], v[216:219], v[156:159], v[52:67]
	ds_read_b64_tr_b16 v[216:217], v174 offset:8704
	ds_read_b64_tr_b16 v[218:219], v174 offset:10752
	s_waitcnt lgkmcnt(6)
	v_mfma_f32_32x32x16_bf16 v[52:67], v[220:223], v[160:163], v[52:67]
	ds_read_b64_tr_b16 v[220:221], v174 offset:12800
	ds_read_b64_tr_b16 v[222:223], v174 offset:14848
	s_waitcnt lgkmcnt(6)
	v_mfma_f32_32x32x16_bf16 v[36:51], v[208:211], v[140:143], v[36:51]
	ds_read_b64_tr_b16 v[208:209], v174 offset:1024
	ds_read_b64_tr_b16 v[210:211], v174 offset:3072
	s_waitcnt lgkmcnt(6)
	v_mfma_f32_32x32x16_bf16 v[36:51], v[212:215], v[144:147], v[36:51]
	ds_read_b64_tr_b16 v[212:213], v174 offset:5120
	ds_read_b64_tr_b16 v[214:215], v174 offset:7168
	s_waitcnt lgkmcnt(6)
	v_mfma_f32_32x32x16_bf16 v[36:51], v[216:219], v[156:159], v[36:51]
	ds_read_b64_tr_b16 v[216:217], v174 offset:9216
	ds_read_b64_tr_b16 v[218:219], v174 offset:11264
	s_waitcnt lgkmcnt(6)
	v_mfma_f32_32x32x16_bf16 v[36:51], v[220:223], v[160:163], v[36:51]
	ds_read_b64_tr_b16 v[220:221], v174 offset:13312
	ds_read_b64_tr_b16 v[222:223], v174 offset:15360
	s_waitcnt lgkmcnt(6)
	v_mfma_f32_32x32x16_bf16 v[20:35], v[208:211], v[140:143], v[20:35]
	ds_read_b64_tr_b16 v[208:209], v174 offset:1536
	ds_read_b64_tr_b16 v[210:211], v174 offset:3584
	s_waitcnt lgkmcnt(6)
	v_mfma_f32_32x32x16_bf16 v[20:35], v[212:215], v[144:147], v[20:35]
	ds_read_b64_tr_b16 v[212:213], v174 offset:5632
	ds_read_b64_tr_b16 v[214:215], v174 offset:7680
	s_waitcnt lgkmcnt(6)
	v_mfma_f32_32x32x16_bf16 v[20:35], v[216:219], v[156:159], v[20:35]
	ds_read_b64_tr_b16 v[216:217], v174 offset:9728
	ds_read_b64_tr_b16 v[218:219], v174 offset:11776
	s_waitcnt lgkmcnt(6)
	v_mfma_f32_32x32x16_bf16 v[20:35], v[220:223], v[160:163], v[20:35]
	ds_read_b64_tr_b16 v[220:221], v174 offset:13824
	ds_read_b64_tr_b16 v[222:223], v174 offset:15872
	s_waitcnt lgkmcnt(6)
	v_mfma_f32_32x32x16_bf16 v[4:19], v[208:211], v[140:143], v[4:19]
	s_waitcnt lgkmcnt(4)
	v_mfma_f32_32x32x16_bf16 v[4:19], v[212:215], v[144:147], v[4:19]
	s_waitcnt lgkmcnt(2)
	v_mfma_f32_32x32x16_bf16 v[4:19], v[216:219], v[156:159], v[4:19]
	s_waitcnt lgkmcnt(0)
	v_mfma_f32_32x32x16_bf16 v[4:19], v[220:223], v[160:163], v[4:19]
	s_setprio 0
	s_branch .Ltail2_a1b0

.LBB0_1454:
	v_max_f32_e32 v2, v167, v167
	v_max_f32_e32 v68, v166, v166
	v_max_f32_e32 v2, v68, v2
	v_max3_f32 v2, v2, v160, v161
	v_max3_f32 v2, v2, v154, v155
	v_max3_f32 v2, v2, v150, v151
	v_max3_f32 v2, v2, v144, v145
	v_max3_f32 v2, v2, v146, v147
	v_max3_f32 v2, v2, v142, v143
	v_max3_f32 v2, v2, v140, v141
	v_max3_f32 v2, v2, v170, v171
	v_max3_f32 v2, v2, v168, v169
	v_max3_f32 v2, v2, v164, v165
	v_max3_f32 v2, v2, v162, v163
	v_max3_f32 v2, v2, v156, v157
	v_max3_f32 v2, v2, v158, v159
	v_max3_f32 v2, v2, v152, v153
	v_max3_f32 v2, v2, v148, v149
	v_mov_b32_e32 v68, v2
	s_nop 1
	v_permlane32_swap_b32_e32 v2, v68
	v_max_f32_e32 v68, v68, v68
	v_max_f32_e32 v2, v2, v2
	v_max_f32_e32 v68, v2, v68
	s_mov_b32 s42, 0xc2800000
	v_cmp_gt_f32_e32 vcc, s42, v68
	s_mov_b64 s[58:59], -1
	s_nop 0
	v_cndmask_b32_e32 v2, 0, v68, vcc
	v_cndmask_b32_e64 v2, v193, v2, s[10:11]
	v_sub_f32_e32 v69, v68, v2
	v_cmp_ge_f32_e32 vcc, s27, v69
	s_cmp_eq_u64 vcc, exec
	v_max_f32_e32 v69, v2, v2
	v_max_f32_e32 v193, v69, v68
	s_cselect_b64 s[10:11], -1, 0
	v_cndmask_b32_e64 v192, v193, v2, s[10:11]
	v_cmp_eq_f32_e32 vcc, 0, v192
	s_cmp_eq_u64 vcc, exec
	s_cselect_b32 s101, 1, 0
	s_cbranch_scc1 .LBB0_1456
	v_sub_f32_e32 v68, v166, v192
	v_exp_f32_e32 v84, v68
	v_sub_f32_e32 v68, v170, v192
	v_sub_f32_e32 v69, v167, v192
	v_exp_f32_e32 v68, v68
	v_exp_f32_e32 v85, v69
	v_sub_f32_e32 v69, v171, v192
	v_sub_f32_e32 v70, v160, v192
	v_exp_f32_e32 v69, v69
	v_exp_f32_e32 v86, v70
	v_sub_f32_e32 v70, v168, v192
	v_exp_f32_e32 v70, v70
	v_add_f32_e32 v71, v68, v84
	v_add_f32_e32 v87, 0, v71
	v_add_f32_e32 v71, v69, v85
	v_pk_add_f32 v[72:73], v[70:71], v[86:87]
	v_sub_f32_e32 v71, v161, v192
	v_pk_add_f32 v[88:89], v[72:73], v[72:73] op_sel_hi:[0,1]
	v_exp_f32_e32 v87, v71
	v_sub_f32_e32 v71, v169, v192
	v_sub_f32_e32 v72, v154, v192
	v_exp_f32_e32 v71, v71
	v_exp_f32_e32 v88, v72
	v_sub_f32_e32 v72, v164, v192
	v_exp_f32_e32 v72, v72
	v_add_f32_e32 v73, v71, v87
	s_mov_b64 s[58:59], 0
	v_pk_add_f32 v[74:75], v[72:73], v[88:89]
	v_sub_f32_e32 v73, v155, v192
	v_pk_add_f32 v[90:91], v[74:75], v[74:75] op_sel_hi:[0,1]
	v_exp_f32_e32 v89, v73
	v_sub_f32_e32 v73, v165, v192
	v_sub_f32_e32 v74, v150, v192
	v_exp_f32_e32 v73, v73
	v_exp_f32_e32 v90, v74
	v_sub_f32_e32 v74, v162, v192
	v_exp_f32_e32 v74, v74
	v_add_f32_e32 v75, v73, v89
	v_pk_add_f32 v[76:77], v[74:75], v[90:91]
	v_sub_f32_e32 v75, v151, v192
	v_pk_add_f32 v[92:93], v[76:77], v[76:77] op_sel_hi:[0,1]
	v_exp_f32_e32 v91, v75
	v_sub_f32_e32 v75, v163, v192
	v_sub_f32_e32 v76, v144, v192
	v_exp_f32_e32 v75, v75
	v_exp_f32_e32 v92, v76
	v_sub_f32_e32 v76, v156, v192
	v_exp_f32_e32 v76, v76
	v_add_f32_e32 v77, v75, v91
	v_pk_add_f32 v[78:79], v[76:77], v[92:93]
	v_sub_f32_e32 v77, v145, v192
	v_pk_add_f32 v[94:95], v[78:79], v[78:79] op_sel_hi:[0,1]
	v_exp_f32_e32 v93, v77
	v_sub_f32_e32 v77, v157, v192
	v_sub_f32_e32 v78, v146, v192
	v_exp_f32_e32 v77, v77
	v_exp_f32_e32 v94, v78
	v_sub_f32_e32 v78, v158, v192
	v_exp_f32_e32 v78, v78
	v_add_f32_e32 v79, v77, v93
	v_pk_add_f32 v[80:81], v[78:79], v[94:95]
	v_sub_f32_e32 v79, v147, v192
	v_pk_add_f32 v[96:97], v[80:81], v[80:81] op_sel_hi:[0,1]
	v_exp_f32_e32 v95, v79
	v_sub_f32_e32 v79, v159, v192
	v_sub_f32_e32 v80, v142, v192
	v_exp_f32_e32 v79, v79
	v_exp_f32_e32 v96, v80
	v_sub_f32_e32 v80, v152, v192
	v_exp_f32_e32 v80, v80
	v_add_f32_e32 v81, v79, v95
	v_pk_add_f32 v[82:83], v[80:81], v[96:97]
	v_sub_f32_e32 v81, v143, v192
	v_pk_add_f32 v[98:99], v[82:83], v[82:83] op_sel_hi:[0,1]
	v_exp_f32_e32 v97, v81
	v_sub_f32_e32 v81, v153, v192
	v_sub_f32_e32 v82, v140, v192
	v_exp_f32_e32 v81, v81
	v_exp_f32_e32 v98, v82
	v_sub_f32_e32 v82, v148, v192
	v_exp_f32_e32 v82, v82
	v_add_f32_e32 v83, v81, v97
	v_pk_add_f32 v[194:195], v[82:83], v[98:99]
	v_sub_f32_e32 v83, v141, v192
	v_exp_f32_e32 v99, v83
	v_add_f32_e32 v194, v194, v195
	v_sub_f32_e32 v83, v149, v192

.LBB0_1467:
	s_add_i32 s98, s18, 64
	s_cmp_le_i32 s98, s40
	s_cbranch_scc0 .Lorig_a1b1
	s_setprio 3
	ds_read_b128 v[140:143], v177
	ds_read_b128 v[144:147], v177 offset:32
	ds_read_b128 v[148:151], v177 offset:64
	ds_read_b128 v[152:155], v177 offset:96
	ds_read_b128 v[208:211], v172 offset:49152
	ds_read_b128 v[212:215], v206 offset:49152
	ds_read_b128 v[216:219], v207 offset:49152
	ds_read_b128 v[220:223], v237 offset:49152
	ds_read_b128 v[224:227], v244 offset:49152
	ds_read_b128 v[228:231], v245 offset:49152
	ds_read_b128 v[232:235], v246 offset:49152
	ds_read_b128 v[238:241], v247 offset:49152
	ds_read_b128 v[156:159], v177 offset:128
	ds_read_b128 v[160:163], v177 offset:160
	ds_read_b128 v[164:167], v177 offset:192
	ds_read_b128 v[168:171], v177 offset:224
	s_waitcnt lgkmcnt(11)
	v_mfma_f32_32x32x16_bf16 v[84:99], v[208:211], v[100:103], v[140:155]
	ds_read_b128 v[208:211], v172 offset:57344
	s_waitcnt lgkmcnt(11)
	v_mfma_f32_32x32x16_bf16 v[84:99], v[212:215], v[104:107], v[84:99]
	ds_read_b128 v[212:215], v206 offset:57344
	s_waitcnt lgkmcnt(11)
	v_mfma_f32_32x32x16_bf16 v[84:99], v[216:219], v[108:111], v[84:99]
	ds_read_b128 v[216:219], v207 offset:57344
	s_waitcnt lgkmcnt(11)
	v_mfma_f32_32x32x16_bf16 v[84:99], v[220:223], v[112:115], v[84:99]
	ds_read_b128 v[220:223], v237 offset:57344
	s_waitcnt lgkmcnt(11)
	v_mfma_f32_32x32x16_bf16 v[84:99], v[224:227], v[116:119], v[84:99]
	ds_read_b128 v[224:227], v244 offset:57344
	s_waitcnt lgkmcnt(11)
	v_mfma_f32_32x32x16_bf16 v[84:99], v[228:231], v[120:123], v[84:99]
	ds_read_b128 v[228:231], v245 offset:57344
	s_waitcnt lgkmcnt(11)
	v_mfma_f32_32x32x16_bf16 v[84:99], v[232:235], v[124:127], v[84:99]
	ds_read_b128 v[232:235], v246 offset:57344
	s_waitcnt lgkmcnt(11)
	v_mfma_f32_32x32x16_bf16 v[84:99], v[238:241], v[128:131], v[84:99]
	ds_read_b128 v[238:241], v247 offset:57344
	s_waitcnt lgkmcnt(7)
	v_mfma_f32_32x32x16_bf16 v[68:83], v[208:211], v[100:103], v[156:171]
	s_waitcnt lgkmcnt(6)
	v_mfma_f32_32x32x16_bf16 v[68:83], v[212:215], v[104:107], v[68:83]
	s_waitcnt lgkmcnt(5)
	v_mfma_f32_32x32x16_bf16 v[68:83], v[216:219], v[108:111], v[68:83]
	s_waitcnt lgkmcnt(4)
	v_mfma_f32_32x32x16_bf16 v[68:83], v[220:223], v[112:115], v[68:83]
	s_waitcnt lgkmcnt(3)
	v_mfma_f32_32x32x16_bf16 v[68:83], v[224:227], v[116:119], v[68:83]
	s_waitcnt lgkmcnt(2)
	v_mfma_f32_32x32x16_bf16 v[68:83], v[228:231], v[120:123], v[68:83]
	s_waitcnt lgkmcnt(1)
	v_mfma_f32_32x32x16_bf16 v[68:83], v[232:235], v[124:127], v[68:83]
	s_waitcnt lgkmcnt(0)
	v_mfma_f32_32x32x16_bf16 v[68:83], v[238:241], v[128:131], v[68:83]
	ds_read_b64_tr_b16 v[208:209], v174 offset:16384
	ds_read_b64_tr_b16 v[210:211], v174 offset:18432
	ds_read_b64_tr_b16 v[212:213], v174 offset:20480
	ds_read_b64_tr_b16 v[214:215], v174 offset:22528
	ds_read_b64_tr_b16 v[216:217], v174 offset:24576
	ds_read_b64_tr_b16 v[218:219], v174 offset:26624
	ds_read_b64_tr_b16 v[220:221], v174 offset:28672
	ds_read_b64_tr_b16 v[222:223], v174 offset:30720
	s_setprio 0
	s_nop 2
	s_cmp_eq_u32 s101, 1
	s_cbranch_scc0 .Lsub_a1b1
	v_exp_f32_e32 v140, v84
	v_exp_f32_e32 v141, v85
	v_exp_f32_e32 v142, v86
	v_exp_f32_e32 v143, v87
	v_exp_f32_e32 v144, v88
	v_exp_f32_e32 v145, v89
	v_exp_f32_e32 v146, v90
	v_exp_f32_e32 v147, v91
	v_exp_f32_e32 v148, v92
	v_exp_f32_e32 v149, v93
	v_exp_f32_e32 v150, v94
	v_exp_f32_e32 v151, v95
	v_exp_f32_e32 v152, v96
	v_exp_f32_e32 v153, v97
	v_exp_f32_e32 v154, v98
	v_exp_f32_e32 v155, v99
	v_add_f32_e32 v248, v140, v141
	v_add_f32_e32 v250, v142, v143
	v_add_f32_e32 v248, v248, v144
	v_add_f32_e32 v250, v250, v145
	v_add_f32_e32 v248, v248, v146
	v_add_f32_e32 v250, v250, v147
	v_add_f32_e32 v248, v248, v148
	v_add_f32_e32 v250, v250, v149
	v_add_f32_e32 v248, v248, v150
	v_add_f32_e32 v250, v250, v151
	v_add_f32_e32 v248, v248, v152
	v_add_f32_e32 v250, v250, v153
	v_add_f32_e32 v248, v248, v154
	v_add_f32_e32 v250, v250, v155
	v_add_f32_e32 v248, v248, v250
	v_cvt_pk_bf16_f32 v140, v140, v141
	v_cvt_pk_bf16_f32 v141, v142, v143
	v_cvt_pk_bf16_f32 v142, v144, v145
	v_cvt_pk_bf16_f32 v143, v146, v147
	v_cvt_pk_bf16_f32 v144, v148, v149
	v_cvt_pk_bf16_f32 v145, v150, v151
	v_cvt_pk_bf16_f32 v146, v152, v153
	v_cvt_pk_bf16_f32 v147, v154, v155
	s_nop 1
	v_permlane32_swap_b32_e32 v140, v142
	v_permlane32_swap_b32_e32 v141, v143
	v_permlane32_swap_b32_e32 v144, v146
	v_permlane32_swap_b32_e32 v145, v147
	v_exp_f32_e32 v156, v68
	v_exp_f32_e32 v157, v69
	v_exp_f32_e32 v158, v70
	v_exp_f32_e32 v159, v71
	v_exp_f32_e32 v160, v72
	v_exp_f32_e32 v161, v73
	v_exp_f32_e32 v162, v74
	v_exp_f32_e32 v163, v75
	v_exp_f32_e32 v164, v76
	v_exp_f32_e32 v165, v77
	v_exp_f32_e32 v166, v78
	v_exp_f32_e32 v167, v79
	v_exp_f32_e32 v168, v80
	v_exp_f32_e32 v169, v81
	v_exp_f32_e32 v170, v82
	v_exp_f32_e32 v171, v83
	v_add_f32_e32 v249, v156, v157
	v_add_f32_e32 v250, v158, v159
	v_add_f32_e32 v249, v249, v160
	v_add_f32_e32 v250, v250, v161
	v_add_f32_e32 v249, v249, v162
	v_add_f32_e32 v250, v250, v163
	v_add_f32_e32 v249, v249, v164
	v_add_f32_e32 v250, v250, v165
	v_add_f32_e32 v249, v249, v166
	v_add_f32_e32 v250, v250, v167
	v_add_f32_e32 v249, v249, v168
	v_add_f32_e32 v250, v250, v169
	v_add_f32_e32 v249, v249, v170
	v_add_f32_e32 v250, v250, v171
	v_add_f32_e32 v249, v249, v250
	v_cvt_pk_bf16_f32 v156, v156, v157
	v_cvt_pk_bf16_f32 v157, v158, v159
	v_cvt_pk_bf16_f32 v158, v160, v161
	v_cvt_pk_bf16_f32 v159, v162, v163
	v_cvt_pk_bf16_f32 v160, v164, v165
	v_cvt_pk_bf16_f32 v161, v166, v167
	v_cvt_pk_bf16_f32 v162, v168, v169
	v_cvt_pk_bf16_f32 v163, v170, v171
	s_nop 1
	v_permlane32_swap_b32_e32 v156, v158
	v_permlane32_swap_b32_e32 v157, v159
	v_permlane32_swap_b32_e32 v160, v162
	v_permlane32_swap_b32_e32 v161, v163
	s_branch .Lsum_a1b1

.Lsum_a1b1:
	v_add_f32_e32 v248, v248, v249
	v_cmp_gt_f32_e32 vcc, 0x5f800000, v248
	v_mov_b32_e32 v249, v248
	s_nop 1
	v_permlane32_swap_b32_e32 v248, v249
	v_add_f32_e32 v248, v248, v249
	s_cmp_eq_u64 vcc, exec
	s_cbranch_scc0 .Lfb_a1b1
	v_add_f32_e32 v191, v248, v191
	v_mov_b32_e32 v193, v192
	s_setprio 3
	s_waitcnt lgkmcnt(6)
	v_mfma_f32_32x32x16_bf16 v[52:67], v[208:211], v[140:143], v[52:67]
	ds_read_b64_tr_b16 v[208:209], v174 offset:16896
	ds_read_b64_tr_b16 v[210:211], v174 offset:18944
	s_waitcnt lgkmcnt(6)
	v_mfma_f32_32x32x16_bf16 v[52:67], v[212:215], v[144:147], v[52:67]
	ds_read_b64_tr_b16 v[212:213], v174 offset:20992
	ds_read_b64_tr_b16 v[214:215], v174 offset:23040
	s_waitcnt lgkmcnt(6)
	v_mfma_f32_32x32x16_bf16 v[52:67], v[216:219], v[156:159], v[52:67]
	ds_read_b64_tr_b16 v[216:217], v174 offset:25088
	ds_read_b64_tr_b16 v[218:219], v174 offset:27136
	s_waitcnt lgkmcnt(6)
	v_mfma_f32_32x32x16_bf16 v[52:67], v[220:223], v[160:163], v[52:67]
	ds_read_b64_tr_b16 v[220:221], v174 offset:29184
	ds_read_b64_tr_b16 v[222:223], v174 offset:31232
	s_waitcnt lgkmcnt(6)
	v_mfma_f32_32x32x16_bf16 v[36:51], v[208:211], v[140:143], v[36:51]
	ds_read_b64_tr_b16 v[208:209], v174 offset:17408
	ds_read_b64_tr_b16 v[210:211], v174 offset:19456
	s_waitcnt lgkmcnt(6)
	v_mfma_f32_32x32x16_bf16 v[36:51], v[212:215], v[144:147], v[36:51]
	ds_read_b64_tr_b16 v[212:213], v174 offset:21504
	ds_read_b64_tr_b16 v[214:215], v174 offset:23552
	s_waitcnt lgkmcnt(6)
	v_mfma_f32_32x32x16_bf16 v[36:51], v[216:219], v[156:159], v[36:51]
	ds_read_b64_tr_b16 v[216:217], v174 offset:25600
	ds_read_b64_tr_b16 v[218:219], v174 offset:27648
	s_waitcnt lgkmcnt(6)
	v_mfma_f32_32x32x16_bf16 v[36:51], v[220:223], v[160:163], v[36:51]
	ds_read_b64_tr_b16 v[220:221], v174 offset:29696
	ds_read_b64_tr_b16 v[222:223], v174 offset:31744
	s_waitcnt lgkmcnt(6)
	v_mfma_f32_32x32x16_bf16 v[20:35], v[208:211], v[140:143], v[20:35]
	ds_read_b64_tr_b16 v[208:209], v174 offset:17920
	ds_read_b64_tr_b16 v[210:211], v174 offset:19968
	s_waitcnt lgkmcnt(6)
	v_mfma_f32_32x32x16_bf16 v[20:35], v[212:215], v[144:147], v[20:35]
	ds_read_b64_tr_b16 v[212:213], v174 offset:22016
	ds_read_b64_tr_b16 v[214:215], v174 offset:24064
	s_waitcnt lgkmcnt(6)
	v_mfma_f32_32x32x16_bf16 v[20:35], v[216:219], v[156:159], v[20:35]
	ds_read_b64_tr_b16 v[216:217], v174 offset:26112
	ds_read_b64_tr_b16 v[218:219], v174 offset:28160
	s_waitcnt lgkmcnt(6)
	v_mfma_f32_32x32x16_bf16 v[20:35], v[220:223], v[160:163], v[20:35]
	ds_read_b64_tr_b16 v[220:221], v174 offset:30208
	ds_read_b64_tr_b16 v[222:223], v174 offset:32256
	s_waitcnt lgkmcnt(6)
	v_mfma_f32_32x32x16_bf16 v[4:19], v[208:211], v[140:143], v[4:19]
	s_waitcnt lgkmcnt(4)
	v_mfma_f32_32x32x16_bf16 v[4:19], v[212:215], v[144:147], v[4:19]
	s_waitcnt lgkmcnt(2)
	v_mfma_f32_32x32x16_bf16 v[4:19], v[216:219], v[156:159], v[4:19]
	s_waitcnt lgkmcnt(0)
	v_mfma_f32_32x32x16_bf16 v[4:19], v[220:223], v[160:163], v[4:19]
	s_setprio 0
	s_branch .Ltail2_a1b1

.LBB0_1469:
	v_max_f32_e32 v2, v167, v167
	v_max_f32_e32 v68, v166, v166
	v_max_f32_e32 v2, v68, v2
	v_max3_f32 v2, v2, v160, v161
	v_max3_f32 v2, v2, v154, v155
	v_max3_f32 v2, v2, v150, v151
	v_max3_f32 v2, v2, v144, v145
	v_max3_f32 v2, v2, v146, v147
	v_max3_f32 v2, v2, v142, v143
	v_max3_f32 v2, v2, v140, v141
	v_max3_f32 v2, v2, v170, v171
	v_max3_f32 v2, v2, v168, v169
	v_max3_f32 v2, v2, v164, v165
	v_max3_f32 v2, v2, v162, v163
	v_max3_f32 v2, v2, v156, v157
	v_max3_f32 v2, v2, v158, v159
	v_max3_f32 v2, v2, v152, v153
	v_max3_f32 v2, v2, v148, v149
	v_mov_b32_e32 v68, v2
	s_nop 1
	v_permlane32_swap_b32_e32 v2, v68
	v_max_f32_e32 v68, v68, v68
	v_max_f32_e32 v2, v2, v2
	v_max_f32_e32 v2, v2, v68
	v_sub_f32_e32 v68, v2, v192
	v_cmp_ge_f32_e32 vcc, s27, v68
	s_cmp_eq_u64 vcc, exec
	v_max_f32_e32 v68, v192, v192
	v_max_f32_e32 v2, v68, v2
	s_cselect_b64 s[8:9], -1, 0
	v_cndmask_b32_e64 v193, v2, v192, s[8:9]
	v_cmp_eq_f32_e32 vcc, 0, v193
	s_cmp_eq_u64 vcc, exec
	s_cselect_b32 s101, 1, 0
	s_mov_b64 s[58:59], -1
	s_cbranch_scc1 .LBB0_1471
	v_sub_f32_e32 v68, v166, v193
	v_exp_f32_e32 v84, v68
	v_sub_f32_e32 v68, v170, v193
	v_sub_f32_e32 v69, v167, v193
	v_exp_f32_e32 v68, v68
	v_exp_f32_e32 v85, v69
	v_sub_f32_e32 v69, v171, v193
	v_sub_f32_e32 v70, v160, v193
	v_exp_f32_e32 v69, v69
	v_exp_f32_e32 v86, v70
	v_sub_f32_e32 v70, v168, v193
	v_exp_f32_e32 v70, v70
	v_add_f32_e32 v71, v68, v84
	v_add_f32_e32 v87, 0, v71
	v_add_f32_e32 v71, v69, v85
	v_pk_add_f32 v[72:73], v[70:71], v[86:87]
	v_sub_f32_e32 v71, v161, v193
	v_pk_add_f32 v[88:89], v[72:73], v[72:73] op_sel_hi:[0,1]
	v_exp_f32_e32 v87, v71
	v_sub_f32_e32 v71, v169, v193
	v_sub_f32_e32 v72, v154, v193
	v_exp_f32_e32 v71, v71
	v_exp_f32_e32 v88, v72
	v_sub_f32_e32 v72, v164, v193
	v_exp_f32_e32 v72, v72
	v_add_f32_e32 v73, v71, v87
	s_mov_b64 s[58:59], 0
	v_pk_add_f32 v[74:75], v[72:73], v[88:89]
	v_sub_f32_e32 v73, v155, v193
	v_pk_add_f32 v[90:91], v[74:75], v[74:75] op_sel_hi:[0,1]
	v_exp_f32_e32 v89, v73
	v_sub_f32_e32 v73, v165, v193
	v_sub_f32_e32 v74, v150, v193
	v_exp_f32_e32 v73, v73
	v_exp_f32_e32 v90, v74
	v_sub_f32_e32 v74, v162, v193
	v_exp_f32_e32 v74, v74
	v_add_f32_e32 v75, v73, v89
	v_pk_add_f32 v[76:77], v[74:75], v[90:91]
	v_sub_f32_e32 v75, v151, v193
	v_pk_add_f32 v[92:93], v[76:77], v[76:77] op_sel_hi:[0,1]
	v_exp_f32_e32 v91, v75
	v_sub_f32_e32 v75, v163, v193
	v_sub_f32_e32 v76, v144, v193
	v_exp_f32_e32 v75, v75
	v_exp_f32_e32 v92, v76
	v_sub_f32_e32 v76, v156, v193
	v_exp_f32_e32 v76, v76
	v_add_f32_e32 v77, v75, v91
	v_pk_add_f32 v[78:79], v[76:77], v[92:93]
	v_sub_f32_e32 v77, v145, v193
	v_pk_add_f32 v[94:95], v[78:79], v[78:79] op_sel_hi:[0,1]
	v_exp_f32_e32 v93, v77
	v_sub_f32_e32 v77, v157, v193
	v_sub_f32_e32 v78, v146, v193
	v_exp_f32_e32 v77, v77
	v_exp_f32_e32 v94, v78
	v_sub_f32_e32 v78, v158, v193
	v_exp_f32_e32 v78, v78
	v_add_f32_e32 v79, v77, v93
	v_pk_add_f32 v[80:81], v[78:79], v[94:95]
	v_sub_f32_e32 v79, v147, v193
	v_pk_add_f32 v[96:97], v[80:81], v[80:81] op_sel_hi:[0,1]
	v_exp_f32_e32 v95, v79
	v_sub_f32_e32 v79, v159, v193
	v_sub_f32_e32 v80, v142, v193
	v_exp_f32_e32 v79, v79
	v_exp_f32_e32 v96, v80
	v_sub_f32_e32 v80, v152, v193
	v_exp_f32_e32 v80, v80
	v_add_f32_e32 v81, v79, v95
	v_pk_add_f32 v[82:83], v[80:81], v[96:97]
	v_sub_f32_e32 v81, v143, v193
	v_pk_add_f32 v[98:99], v[82:83], v[82:83] op_sel_hi:[0,1]
	v_exp_f32_e32 v97, v81
	v_sub_f32_e32 v81, v153, v193
	v_sub_f32_e32 v82, v140, v193
	v_exp_f32_e32 v81, v81
	v_exp_f32_e32 v98, v82
	v_sub_f32_e32 v82, v148, v193
	v_exp_f32_e32 v82, v82
	v_add_f32_e32 v83, v81, v97
	v_pk_add_f32 v[194:195], v[82:83], v[98:99]
	v_sub_f32_e32 v83, v141, v193
	v_exp_f32_e32 v99, v83
	v_add_f32_e32 v194, v194, v195
	v_sub_f32_e32 v83, v149, v193
